# attention O rows stored with the nt hint (streaming: less dirty L2 residue to write back at the phase seam)
# speedup vs baseline: 1.0098x; 1.0045x over previous
.LBB0_485:
	s_waitcnt vmcnt(0)
	s_barrier
	s_waitcnt lgkmcnt(0)
	v_add_f32_e32 v34, v59, v60
	v_div_scale_f32 v35, s[4:5], v34, v34, 1.0
	v_rcp_f32_e32 v36, v35
	v_div_scale_f32 v37, vcc, 1.0, v34, 1.0
	s_ashr_i32 s87, s86, 31
	v_fma_f32 v38, -v35, v36, 1.0
	v_fmac_f32_e32 v36, v38, v36
	v_mul_f32_e32 v38, v37, v36
	v_fma_f32 v39, -v35, v38, v37
	v_fmac_f32_e32 v38, v39, v36
	v_fma_f32 v35, -v35, v38, v37
	v_div_fmas_f32 v35, v35, v36, v38
	v_div_fixup_f32 v35, v35, v34, 1.0
	v_mul_f32_e32 v18, v35, v18
	v_mul_f32_e32 v19, v35, v19
	v_cvt_pk_bf16_f32 v18, v18, v19
	v_mul_f32_e32 v19, v35, v20
	v_mul_f32_e32 v20, v35, v21
	v_cvt_pk_bf16_f32 v19, v19, v20
	v_add_u32_e32 v20, v194, v193
	ds_write_b64 v20, v[18:19] offset:4096
	v_mul_f32_e32 v18, v35, v22
	v_mul_f32_e32 v19, v35, v23
	v_cvt_pk_bf16_f32 v18, v18, v19
	v_mul_f32_e32 v19, v35, v24
	v_mul_f32_e32 v20, v35, v25
	v_cvt_pk_bf16_f32 v19, v19, v20
	ds_write_b64 v210, v[18:19] offset:4096
	v_mul_f32_e32 v18, v35, v26
	v_mul_f32_e32 v19, v35, v27
	v_cvt_pk_bf16_f32 v18, v18, v19
	v_mul_f32_e32 v19, v35, v28
	v_mul_f32_e32 v20, v35, v29
	v_cvt_pk_bf16_f32 v19, v19, v20
	ds_write_b64 v211, v[18:19] offset:4096
	v_mul_f32_e32 v18, v35, v30
	v_mul_f32_e32 v19, v35, v31
	v_cvt_pk_bf16_f32 v18, v18, v19
	v_mul_f32_e32 v19, v35, v32
	v_mul_f32_e32 v2, v35, v2
	v_mul_f32_e32 v3, v35, v3
	v_mul_f32_e32 v20, v35, v33
	v_cvt_pk_bf16_f32 v19, v19, v20
	ds_write_b64 v212, v[18:19] offset:4096
	v_cvt_pk_bf16_f32 v2, v2, v3
	v_mul_f32_e32 v3, v35, v4
	v_mul_f32_e32 v4, v35, v5
	v_cvt_pk_bf16_f32 v3, v3, v4
	ds_write_b64 v213, v[2:3] offset:4096
	v_mul_f32_e32 v2, v35, v6
	v_mul_f32_e32 v3, v35, v7
	v_cvt_pk_bf16_f32 v2, v2, v3
	v_mul_f32_e32 v3, v35, v8
	v_mul_f32_e32 v4, v35, v9
	v_cvt_pk_bf16_f32 v3, v3, v4
	ds_write_b64 v214, v[2:3] offset:4096
	v_mul_f32_e32 v2, v35, v10
	v_mul_f32_e32 v3, v35, v11
	v_cvt_pk_bf16_f32 v2, v2, v3
	v_mul_f32_e32 v3, v35, v12
	v_mul_f32_e32 v4, v35, v13
	v_cvt_pk_bf16_f32 v3, v3, v4
	ds_write_b64 v215, v[2:3] offset:4096
	v_mul_f32_e32 v2, v35, v14
	v_mul_f32_e32 v3, v35, v15
	v_cvt_pk_bf16_f32 v2, v2, v3
	v_mul_f32_e32 v3, v35, v16
	v_mul_f32_e32 v4, v35, v17
	v_cvt_pk_bf16_f32 v3, v3, v4
	ds_write_b64 v216, v[2:3] offset:4096
	s_lshl_b64 s[4:5], s[86:87], 14
	s_ashr_i32 s43, s42, 31
	s_add_u32 s4, s4, s42
	ds_read_b128 v[2:5], v217 offset:4096
	v_mul_lo_u32 v6, s81, v203
	s_addc_u32 s5, s5, s43
	v_ashrrev_i32_e32 v7, 31, v6
	s_lshl_b32 s90, s37, 1
	v_lshl_add_u64 v[6:7], s[4:5], 0, v[6:7]
	v_lshl_add_u64 v[10:11], v[184:185], 0, s[90:91]
	v_lshlrev_b64 v[6:7], 11, v[6:7]
	v_lshl_add_u64 v[12:13], v[10:11], 0, v[6:7]
	ds_read_b128 v[6:9], v218 offset:4096
	s_waitcnt lgkmcnt(0)
	global_store_dwordx4 v[12:13], v[2:5], off nt
	s_nop 1
	v_mul_lo_u32 v2, s81, v204
	v_ashrrev_i32_e32 v3, 31, v2
	v_lshl_add_u64 v[2:3], s[4:5], 0, v[2:3]
	v_lshlrev_b64 v[2:3], 11, v[2:3]
	v_lshl_add_u64 v[2:3], v[10:11], 0, v[2:3]
	global_store_dwordx4 v[2:3], v[6:9], off nt
	ds_read_b128 v[2:5], v219 offset:4096
	s_nop 0
	v_mul_lo_u32 v6, s81, v205
	v_ashrrev_i32_e32 v7, 31, v6
	v_lshl_add_u64 v[6:7], s[4:5], 0, v[6:7]
	v_lshlrev_b64 v[6:7], 11, v[6:7]
	v_lshl_add_u64 v[12:13], v[10:11], 0, v[6:7]
	ds_read_b128 v[6:9], v220 offset:4096
	s_waitcnt lgkmcnt(0)
	global_store_dwordx4 v[12:13], v[2:5], off nt
	s_nop 1
	v_mul_lo_u32 v2, s81, v206
	v_ashrrev_i32_e32 v3, 31, v2
	v_lshl_add_u64 v[2:3], s[4:5], 0, v[2:3]
	v_lshlrev_b64 v[2:3], 11, v[2:3]
	v_lshl_add_u64 v[2:3], v[10:11], 0, v[2:3]
	global_store_dwordx4 v[2:3], v[6:9], off nt
	s_and_saveexec_b64 s[4:5], s[6:7]
	s_cbranch_execz .LBB0_487
	v_log_f32_e32 v2, v34
	s_lshl_b64 s[44:45], s[86:87], 20
	v_readlane_b32 s37, v254, 17
	v_ashrrev_i32_e32 v181, 31, v180
	v_add_f32_e32 v2, v66, v2
	s_add_u32 s44, s37, s44
	v_readlane_b32 s37, v254, 18
	v_mul_f32_e32 v4, 0x3f317218, v2
	s_addc_u32 s45, s37, s45
	v_lshlrev_b64 v[2:3], 6, v[180:181]
	s_mov_b32 s89, s91
	v_lshl_add_u64 v[2:3], s[44:45], 0, v[2:3]
	v_lshl_add_u64 v[2:3], s[88:89], 2, v[2:3]
	global_store_dword v[2:3], v4, off
